# speedup vs baseline: 1.0119x; 1.0119x over previous
_Z9l1_kernelPKiS0_P15HIP_vector_typeIjLj2EEPiS4_PKfS6_S6_S6_PfP6__half:
	s_cmp_gt_u32 s2, 42
	s_mov_b64 s[4:5], -1
	s_cbranch_scc0 .LBB0_17
	s_mul_i32 s15, s2, 0xeb
	s_add_i32 s3, s15, 0xffffd887
	s_min_i32 s16, s3, 0xc265
	s_add_i32 s12, s16, 0xeb
	s_cmp_ge_i32 s3, s12
	s_cbranch_scc1 .LBB0_16
	s_load_dwordx4 s[4:7], s[0:1], 0x28
	s_load_dwordx2 s[10:11], s[0:1], 0x38
	s_load_dwordx4 s[24:27], s[0:1], 0x40
	s_load_dwordx2 s[28:29], s[0:1], 0x50
	v_lshlrev_b32_e32 v1, 4, v0
	v_and_b32_e32 v2, 0x1f0, v1
	v_mov_b32_e32 v3, 0
	v_lshrrev_b32_e32 v1, 5, v0
	s_add_i32 s13, s16, 0xea
	s_waitcnt lgkmcnt(0)
	v_lshl_add_u64 v[110:111], s[4:5], 0, v[2:3]
	v_add_u32_e32 v2, s3, v1
	v_min_i32_e32 v2, s13, v2
	v_ashrrev_i32_e32 v3, 31, v2
	v_lshlrev_b64 v[2:3], 9, v[2:3]
	v_lshl_add_u64 v[10:11], v[110:111], 0, v[2:3]
	v_or_b32_e32 v2, 0x200, v0
	v_lshrrev_b32_e32 v146, 5, v2
	v_add_u32_e32 v2, s3, v146
	v_min_i32_e32 v2, s13, v2
	v_ashrrev_i32_e32 v3, 31, v2
	v_lshlrev_b64 v[2:3], 9, v[2:3]
	v_or_b32_e32 v147, 32, v1
	v_lshl_add_u64 v[12:13], v[110:111], 0, v[2:3]
	global_load_dwordx4 v[2:5], v[10:11], off
	global_load_dwordx4 v[6:9], v[12:13], off
	v_add_u32_e32 v10, s3, v147
	v_min_i32_e32 v10, s13, v10
	v_ashrrev_i32_e32 v11, 31, v10
	v_lshlrev_b64 v[10:11], 9, v[10:11]
	v_lshl_add_u64 v[10:11], v[110:111], 0, v[10:11]
	global_load_dwordx4 v[10:13], v[10:11], off
	v_lshrrev_b32_e32 v149, 6, v0
	s_movk_i32 s4, 0x200
	v_and_b32_e32 v150, 15, v0
	v_cmp_gt_u32_e32 vcc, s4, v0
	v_lshlrev_b32_e32 v151, 4, v149
	s_and_saveexec_b64 s[4:5], vcc
	s_xor_b64 s[4:5], exec, s[4:5]
	v_or_b32_e32 v32, v151, v150
	s_or_saveexec_b64 s[4:5], s[4:5]
	v_lshlrev_b32_e32 v14, 1, v150
	v_mov_b64_e32 v[30:31], s[6:7]
	s_xor_b64 exec, exec, s[4:5]
	v_and_b32_e32 v15, 0x60, v151
	v_bfe_u32 v16, v0, 6, 1
	v_or3_b32 v32, v16, v15, v14
	v_mov_b64_e32 v[30:31], s[10:11]
	s_or_b64 exec, exec, s[4:5]
	s_movk_i32 s17, 0x110
	s_mov_b32 s14, 0x7060302
	s_sub_i32 s19, s16, s3
	s_addk_i32 s19, 0x11a
	v_readfirstlane_b32 s30, v149
	v_bfe_u32 v152, v0, 4, 2
	v_lshlrev_b32_e32 v153, 5, v149
	v_and_b32_e32 v153, 0x60, v153
	v_or_b32_e32 v144, v151, v150
	v_lshlrev_b32_e32 v144, 2, v144
	v_lshl_add_u32 v144, v152, 12, v144
	v_lshlrev_b32_e32 v145, 3, v150
	v_lshl_add_u32 v145, v153, 2, v145
	v_lshl_add_u32 v145, v152, 12, v145
	s_waitcnt lgkmcnt(0)
	s_cmp_lt_u32 s30, 4
	s_cselect_b32 s20, s10, s24
	s_cselect_b32 s21, s11, s25
	s_add_u32 s32, s6, 0x4000
	s_addc_u32 s33, s7, 0
	s_add_u32 s34, s6, 0x8000
	s_addc_u32 s35, s7, 0
	s_add_u32 s36, s6, 0xc000
	s_addc_u32 s37, s7, 0
	s_add_u32 s38, s20, 0x4000
	s_addc_u32 s39, s21, 0
	s_add_u32 s40, s20, 0x8000
	s_addc_u32 s41, s21, 0
	s_add_u32 s42, s20, 0xc000
	s_addc_u32 s43, s21, 0
	s_mul_hi_u32 s5, s19, 0xaaaaaaab
	s_addk_i32 s16, 0xfa
	s_lshr_b32 s10, s5, 5
	s_mov_b32 s11, 0
	global_load_dword v112, v144, s[6:7]
	global_load_dword v113, v144, s[6:7] offset:512
	global_load_dword v114, v144, s[6:7] offset:1024
	global_load_dword v115, v144, s[6:7] offset:1536
	global_load_dword v116, v144, s[6:7] offset:2048
	global_load_dword v117, v144, s[6:7] offset:2560
	global_load_dword v118, v144, s[6:7] offset:3072
	global_load_dword v119, v144, s[6:7] offset:3584
	global_load_dwordx2 v[176:177], v145, s[20:21]
	global_load_dwordx2 v[178:179], v145, s[20:21] offset:512
	global_load_dwordx2 v[180:181], v145, s[20:21] offset:1024
	global_load_dwordx2 v[182:183], v145, s[20:21] offset:1536
	global_load_dwordx2 v[184:185], v145, s[20:21] offset:2048
	global_load_dwordx2 v[186:187], v145, s[20:21] offset:2560
	global_load_dwordx2 v[188:189], v145, s[20:21] offset:3072
	global_load_dwordx2 v[190:191], v145, s[20:21] offset:3584
	global_load_dword v120, v144, s[32:33]
	global_load_dword v121, v144, s[32:33] offset:512
	global_load_dword v122, v144, s[32:33] offset:1024
	global_load_dword v123, v144, s[32:33] offset:1536
	global_load_dword v124, v144, s[32:33] offset:2048
	global_load_dword v125, v144, s[32:33] offset:2560
	global_load_dword v126, v144, s[32:33] offset:3072
	global_load_dword v127, v144, s[32:33] offset:3584
	global_load_dwordx2 v[192:193], v145, s[38:39]
	global_load_dwordx2 v[194:195], v145, s[38:39] offset:512
	global_load_dwordx2 v[196:197], v145, s[38:39] offset:1024
	global_load_dwordx2 v[198:199], v145, s[38:39] offset:1536
	global_load_dwordx2 v[200:201], v145, s[38:39] offset:2048
	global_load_dwordx2 v[202:203], v145, s[38:39] offset:2560
	global_load_dwordx2 v[204:205], v145, s[38:39] offset:3072
	global_load_dwordx2 v[206:207], v145, s[38:39] offset:3584
	global_load_dword v128, v144, s[34:35]
	global_load_dword v129, v144, s[34:35] offset:512
	global_load_dword v130, v144, s[34:35] offset:1024
	global_load_dword v131, v144, s[34:35] offset:1536
	global_load_dword v132, v144, s[34:35] offset:2048
	global_load_dword v133, v144, s[34:35] offset:2560
	global_load_dword v134, v144, s[34:35] offset:3072
	global_load_dword v135, v144, s[34:35] offset:3584
	global_load_dwordx2 v[208:209], v145, s[40:41]
	global_load_dwordx2 v[210:211], v145, s[40:41] offset:512
	global_load_dwordx2 v[212:213], v145, s[40:41] offset:1024
	global_load_dwordx2 v[214:215], v145, s[40:41] offset:1536
	global_load_dwordx2 v[216:217], v145, s[40:41] offset:2048
	global_load_dwordx2 v[218:219], v145, s[40:41] offset:2560
	global_load_dwordx2 v[220:221], v145, s[40:41] offset:3072
	global_load_dwordx2 v[222:223], v145, s[40:41] offset:3584
	global_load_dword v136, v144, s[36:37]
	global_load_dword v137, v144, s[36:37] offset:512
	global_load_dword v138, v144, s[36:37] offset:1024
	global_load_dword v139, v144, s[36:37] offset:1536
	global_load_dword v140, v144, s[36:37] offset:2048
	global_load_dword v141, v144, s[36:37] offset:2560
	global_load_dword v142, v144, s[36:37] offset:3072
	global_load_dword v143, v144, s[36:37] offset:3584
	global_load_dwordx2 v[224:225], v145, s[42:43]
	global_load_dwordx2 v[226:227], v145, s[42:43] offset:512
	global_load_dwordx2 v[228:229], v145, s[42:43] offset:1024
	global_load_dwordx2 v[230:231], v145, s[42:43] offset:1536
	global_load_dwordx2 v[232:233], v145, s[42:43] offset:2048
	global_load_dwordx2 v[234:235], v145, s[42:43] offset:2560
	global_load_dwordx2 v[236:237], v145, s[42:43] offset:3072
	global_load_dwordx2 v[238:239], v145, s[42:43] offset:3584
	s_waitcnt vmcnt(60)
	v_and_b32_e32 v242, 0xffff0000, v3
	v_lshlrev_b32_e32 v240, 3, v0
	v_sub_f32_e32 v244, v3, v242
	v_and_b32_e32 v242, 0xffff0000, v4
	v_and_b32_e32 v148, 0xf8, v240
	v_and_b32_e32 v240, 0xffff0000, v2
	v_sub_f32_e32 v245, v4, v242
	v_and_b32_e32 v242, 0xffff0000, v5
	v_sub_f32_e32 v240, v2, v240
	v_sub_f32_e32 v246, v5, v242
	v_mad_u32_u24 v247, v1, s17, v148
	v_perm_b32 v242, v3, v2, s14
	v_perm_b32 v243, v5, v4, s14
	ds_write_b64 v247, v[242:243]
	v_perm_b32 v242, v244, v240, s14
	v_perm_b32 v243, v246, v245, s14
	ds_write_b64 v247, v[242:243] offset:13056
	v_and_b32_e32 v242, 0xffff0000, v7
	v_sub_f32_e32 v244, v7, v242
	v_and_b32_e32 v242, 0xffff0000, v8
	v_and_b32_e32 v240, 0xffff0000, v6
	v_sub_f32_e32 v245, v8, v242
	v_and_b32_e32 v242, 0xffff0000, v9
	v_sub_f32_e32 v240, v6, v240
	v_sub_f32_e32 v246, v9, v242
	v_mad_u32_u24 v241, v146, s17, v148
	v_perm_b32 v242, v7, v6, s14
	v_perm_b32 v243, v9, v8, s14
	ds_write_b64 v241, v[242:243]
	v_perm_b32 v242, v244, v240, s14
	v_perm_b32 v243, v246, v245, s14
	ds_write_b64 v241, v[242:243] offset:13056
	v_and_b32_e32 v242, 0xffff0000, v11
	v_sub_f32_e32 v244, v11, v242
	v_and_b32_e32 v242, 0xffff0000, v12
	v_and_b32_e32 v240, 0xffff0000, v10
	v_sub_f32_e32 v245, v12, v242
	v_and_b32_e32 v242, 0xffff0000, v13
	v_sub_f32_e32 v240, v10, v240
	v_sub_f32_e32 v246, v13, v242
	v_perm_b32 v242, v11, v10, s14
	v_perm_b32 v243, v13, v12, s14
	ds_write_b64 v247, v[242:243] offset:8704
	v_perm_b32 v242, v244, v240, s14
	v_perm_b32 v243, v246, v245, s14
	ds_write_b64 v247, v[242:243] offset:21760
	s_waitcnt lgkmcnt(0)
	s_barrier
	s_waitcnt vmcnt(56)
	v_cvt_pk_bf16_f32 v106, v112, v113
	v_lshlrev_b32_e32 v248, 16, v106
	v_and_b32_e32 v249, 0xffff0000, v106
	v_sub_f32_e32 v248, v112, v248
	v_sub_f32_e32 v249, v113, v249
	v_cvt_pk_bf16_f32 v102, v248, v249
	v_cvt_pk_bf16_f32 v107, v114, v115
	v_lshlrev_b32_e32 v250, 16, v107
	v_and_b32_e32 v251, 0xffff0000, v107
	v_sub_f32_e32 v250, v114, v250
	v_sub_f32_e32 v251, v115, v251
	v_cvt_pk_bf16_f32 v103, v250, v251
	v_cvt_pk_bf16_f32 v108, v116, v117
	v_lshlrev_b32_e32 v248, 16, v108
	v_and_b32_e32 v249, 0xffff0000, v108
	v_sub_f32_e32 v248, v116, v248
	v_sub_f32_e32 v249, v117, v249
	v_cvt_pk_bf16_f32 v104, v248, v249
	v_cvt_pk_bf16_f32 v109, v118, v119
	v_lshlrev_b32_e32 v250, 16, v109
	v_and_b32_e32 v251, 0xffff0000, v109
	v_sub_f32_e32 v250, v118, v250
	v_sub_f32_e32 v251, v119, v251
	v_cvt_pk_bf16_f32 v105, v250, v251
	s_waitcnt vmcnt(48)
	v_cvt_pk_bf16_f32 v74, v176, v178
	v_lshlrev_b32_e32 v248, 16, v74
	v_and_b32_e32 v249, 0xffff0000, v74
	v_sub_f32_e32 v248, v176, v248
	v_sub_f32_e32 v249, v178, v249
	v_cvt_pk_bf16_f32 v70, v248, v249
	v_cvt_pk_bf16_f32 v75, v180, v182
	v_lshlrev_b32_e32 v250, 16, v75
	v_and_b32_e32 v251, 0xffff0000, v75
	v_sub_f32_e32 v250, v180, v250
	v_sub_f32_e32 v251, v182, v251
	v_cvt_pk_bf16_f32 v71, v250, v251
	v_cvt_pk_bf16_f32 v76, v184, v186
	v_lshlrev_b32_e32 v248, 16, v76
	v_and_b32_e32 v249, 0xffff0000, v76
	v_sub_f32_e32 v248, v184, v248
	v_sub_f32_e32 v249, v186, v249
	v_cvt_pk_bf16_f32 v72, v248, v249
	v_cvt_pk_bf16_f32 v77, v188, v190
	v_lshlrev_b32_e32 v250, 16, v77
	v_and_b32_e32 v251, 0xffff0000, v77
	v_sub_f32_e32 v250, v188, v250
	v_sub_f32_e32 v251, v190, v251
	v_cvt_pk_bf16_f32 v73, v250, v251
	v_cvt_pk_bf16_f32 v38, v177, v179
	v_lshlrev_b32_e32 v248, 16, v38
	v_and_b32_e32 v249, 0xffff0000, v38
	v_sub_f32_e32 v248, v177, v248
	v_sub_f32_e32 v249, v179, v249
	v_cvt_pk_bf16_f32 v42, v248, v249
	v_cvt_pk_bf16_f32 v39, v181, v183
	v_lshlrev_b32_e32 v250, 16, v39
	v_and_b32_e32 v251, 0xffff0000, v39
	v_sub_f32_e32 v250, v181, v250
	v_sub_f32_e32 v251, v183, v251
	v_cvt_pk_bf16_f32 v43, v250, v251
	v_cvt_pk_bf16_f32 v40, v185, v187
	v_lshlrev_b32_e32 v248, 16, v40
	v_and_b32_e32 v249, 0xffff0000, v40
	v_sub_f32_e32 v248, v185, v248
	v_sub_f32_e32 v249, v187, v249
	v_cvt_pk_bf16_f32 v44, v248, v249
	v_cvt_pk_bf16_f32 v41, v189, v191
	v_lshlrev_b32_e32 v250, 16, v41
	v_and_b32_e32 v251, 0xffff0000, v41
	v_sub_f32_e32 v250, v189, v250
	v_sub_f32_e32 v251, v191, v251
	v_cvt_pk_bf16_f32 v45, v250, v251
	s_waitcnt vmcnt(40)
	v_cvt_pk_bf16_f32 v98, v120, v121
	v_lshlrev_b32_e32 v248, 16, v98
	v_and_b32_e32 v249, 0xffff0000, v98
	v_sub_f32_e32 v248, v120, v248
	v_sub_f32_e32 v249, v121, v249
	v_cvt_pk_bf16_f32 v94, v248, v249
	v_cvt_pk_bf16_f32 v99, v122, v123
	v_lshlrev_b32_e32 v250, 16, v99
	v_and_b32_e32 v251, 0xffff0000, v99
	v_sub_f32_e32 v250, v122, v250
	v_sub_f32_e32 v251, v123, v251
	v_cvt_pk_bf16_f32 v95, v250, v251
	v_cvt_pk_bf16_f32 v100, v124, v125
	v_lshlrev_b32_e32 v248, 16, v100
	v_and_b32_e32 v249, 0xffff0000, v100
	v_sub_f32_e32 v248, v124, v248
	v_sub_f32_e32 v249, v125, v249
	v_cvt_pk_bf16_f32 v96, v248, v249
	v_cvt_pk_bf16_f32 v101, v126, v127
	v_lshlrev_b32_e32 v250, 16, v101
	v_and_b32_e32 v251, 0xffff0000, v101
	v_sub_f32_e32 v250, v126, v250
	v_sub_f32_e32 v251, v127, v251
	v_cvt_pk_bf16_f32 v97, v250, v251
	s_waitcnt vmcnt(32)
	v_cvt_pk_bf16_f32 v62, v192, v194
	v_lshlrev_b32_e32 v248, 16, v62
	v_and_b32_e32 v249, 0xffff0000, v62
	v_sub_f32_e32 v248, v192, v248
	v_sub_f32_e32 v249, v194, v249
	v_cvt_pk_bf16_f32 v66, v248, v249
	v_cvt_pk_bf16_f32 v63, v196, v198
	v_lshlrev_b32_e32 v250, 16, v63
	v_and_b32_e32 v251, 0xffff0000, v63
	v_sub_f32_e32 v250, v196, v250
	v_sub_f32_e32 v251, v198, v251
	v_cvt_pk_bf16_f32 v67, v250, v251
	v_cvt_pk_bf16_f32 v64, v200, v202
	v_lshlrev_b32_e32 v248, 16, v64
	v_and_b32_e32 v249, 0xffff0000, v64
	v_sub_f32_e32 v248, v200, v248
	v_sub_f32_e32 v249, v202, v249
	v_cvt_pk_bf16_f32 v68, v248, v249
	v_cvt_pk_bf16_f32 v65, v204, v206
	v_lshlrev_b32_e32 v250, 16, v65
	v_and_b32_e32 v251, 0xffff0000, v65
	v_sub_f32_e32 v250, v204, v250
	v_sub_f32_e32 v251, v206, v251
	v_cvt_pk_bf16_f32 v69, v250, v251
	v_cvt_pk_bf16_f32 v30, v193, v195
	v_lshlrev_b32_e32 v248, 16, v30
	v_and_b32_e32 v249, 0xffff0000, v30
	v_sub_f32_e32 v248, v193, v248
	v_sub_f32_e32 v249, v195, v249
	v_cvt_pk_bf16_f32 v34, v248, v249
	v_cvt_pk_bf16_f32 v31, v197, v199
	v_lshlrev_b32_e32 v250, 16, v31
	v_and_b32_e32 v251, 0xffff0000, v31
	v_sub_f32_e32 v250, v197, v250
	v_sub_f32_e32 v251, v199, v251
	v_cvt_pk_bf16_f32 v35, v250, v251
	v_cvt_pk_bf16_f32 v32, v201, v203
	v_lshlrev_b32_e32 v248, 16, v32
	v_and_b32_e32 v249, 0xffff0000, v32
	v_sub_f32_e32 v248, v201, v248
	v_sub_f32_e32 v249, v203, v249
	v_cvt_pk_bf16_f32 v36, v248, v249
	v_cvt_pk_bf16_f32 v33, v205, v207
	v_lshlrev_b32_e32 v250, 16, v33
	v_and_b32_e32 v251, 0xffff0000, v33
	v_sub_f32_e32 v250, v205, v250
	v_sub_f32_e32 v251, v207, v251
	v_cvt_pk_bf16_f32 v37, v250, v251
	s_waitcnt vmcnt(24)
	v_cvt_pk_bf16_f32 v90, v128, v129
	v_lshlrev_b32_e32 v248, 16, v90
	v_and_b32_e32 v249, 0xffff0000, v90
	v_sub_f32_e32 v248, v128, v248
	v_sub_f32_e32 v249, v129, v249
	v_cvt_pk_bf16_f32 v86, v248, v249
	v_cvt_pk_bf16_f32 v91, v130, v131
	v_lshlrev_b32_e32 v250, 16, v91
	v_and_b32_e32 v251, 0xffff0000, v91
	v_sub_f32_e32 v250, v130, v250
	v_sub_f32_e32 v251, v131, v251
	v_cvt_pk_bf16_f32 v87, v250, v251
	v_cvt_pk_bf16_f32 v92, v132, v133
	v_lshlrev_b32_e32 v248, 16, v92
	v_and_b32_e32 v249, 0xffff0000, v92
	v_sub_f32_e32 v248, v132, v248
	v_sub_f32_e32 v249, v133, v249
	v_cvt_pk_bf16_f32 v88, v248, v249
	v_cvt_pk_bf16_f32 v93, v134, v135
	v_lshlrev_b32_e32 v250, 16, v93
	v_and_b32_e32 v251, 0xffff0000, v93
	v_sub_f32_e32 v250, v134, v250
	v_sub_f32_e32 v251, v135, v251
	v_cvt_pk_bf16_f32 v89, v250, v251
	s_waitcnt vmcnt(16)
	v_cvt_pk_bf16_f32 v54, v208, v210
	v_lshlrev_b32_e32 v248, 16, v54
	v_and_b32_e32 v249, 0xffff0000, v54
	v_sub_f32_e32 v248, v208, v248
	v_sub_f32_e32 v249, v210, v249
	v_cvt_pk_bf16_f32 v58, v248, v249
	v_cvt_pk_bf16_f32 v55, v212, v214
	v_lshlrev_b32_e32 v250, 16, v55
	v_and_b32_e32 v251, 0xffff0000, v55
	v_sub_f32_e32 v250, v212, v250
	v_sub_f32_e32 v251, v214, v251
	v_cvt_pk_bf16_f32 v59, v250, v251
	v_cvt_pk_bf16_f32 v56, v216, v218
	v_lshlrev_b32_e32 v248, 16, v56
	v_and_b32_e32 v249, 0xffff0000, v56
	v_sub_f32_e32 v248, v216, v248
	v_sub_f32_e32 v249, v218, v249
	v_cvt_pk_bf16_f32 v60, v248, v249
	v_cvt_pk_bf16_f32 v57, v220, v222
	v_lshlrev_b32_e32 v250, 16, v57
	v_and_b32_e32 v251, 0xffff0000, v57
	v_sub_f32_e32 v250, v220, v250
	v_sub_f32_e32 v251, v222, v251
	v_cvt_pk_bf16_f32 v61, v250, v251
	v_cvt_pk_bf16_f32 v26, v209, v211
	v_lshlrev_b32_e32 v248, 16, v26
	v_and_b32_e32 v249, 0xffff0000, v26
	v_sub_f32_e32 v248, v209, v248
	v_sub_f32_e32 v249, v211, v249
	v_cvt_pk_bf16_f32 v22, v248, v249
	v_cvt_pk_bf16_f32 v27, v213, v215
	v_lshlrev_b32_e32 v250, 16, v27
	v_and_b32_e32 v251, 0xffff0000, v27
	v_sub_f32_e32 v250, v213, v250
	v_sub_f32_e32 v251, v215, v251
	v_cvt_pk_bf16_f32 v23, v250, v251
	v_cvt_pk_bf16_f32 v28, v217, v219
	v_lshlrev_b32_e32 v248, 16, v28
	v_and_b32_e32 v249, 0xffff0000, v28
	v_sub_f32_e32 v248, v217, v248
	v_sub_f32_e32 v249, v219, v249
	v_cvt_pk_bf16_f32 v24, v248, v249
	v_cvt_pk_bf16_f32 v29, v221, v223
	v_lshlrev_b32_e32 v250, 16, v29
	v_and_b32_e32 v251, 0xffff0000, v29
	v_sub_f32_e32 v250, v221, v250
	v_sub_f32_e32 v251, v223, v251
	v_cvt_pk_bf16_f32 v25, v250, v251
	s_waitcnt vmcnt(8)
	v_cvt_pk_bf16_f32 v82, v136, v137
	v_lshlrev_b32_e32 v248, 16, v82
	v_and_b32_e32 v249, 0xffff0000, v82
	v_sub_f32_e32 v248, v136, v248
	v_sub_f32_e32 v249, v137, v249
	v_cvt_pk_bf16_f32 v78, v248, v249
	v_cvt_pk_bf16_f32 v83, v138, v139
	v_lshlrev_b32_e32 v250, 16, v83
	v_and_b32_e32 v251, 0xffff0000, v83
	v_sub_f32_e32 v250, v138, v250
	v_sub_f32_e32 v251, v139, v251
	v_cvt_pk_bf16_f32 v79, v250, v251
	v_cvt_pk_bf16_f32 v84, v140, v141
	v_lshlrev_b32_e32 v248, 16, v84
	v_and_b32_e32 v249, 0xffff0000, v84
	v_sub_f32_e32 v248, v140, v248
	v_sub_f32_e32 v249, v141, v249
	v_cvt_pk_bf16_f32 v80, v248, v249
	v_cvt_pk_bf16_f32 v85, v142, v143
	v_lshlrev_b32_e32 v250, 16, v85
	v_and_b32_e32 v251, 0xffff0000, v85
	v_sub_f32_e32 v250, v142, v250
	v_sub_f32_e32 v251, v143, v251
	v_cvt_pk_bf16_f32 v81, v250, v251
	s_waitcnt vmcnt(0)
	v_cvt_pk_bf16_f32 v46, v224, v226
	v_lshlrev_b32_e32 v248, 16, v46
	v_and_b32_e32 v249, 0xffff0000, v46
	v_sub_f32_e32 v248, v224, v248
	v_sub_f32_e32 v249, v226, v249
	v_cvt_pk_bf16_f32 v50, v248, v249
	v_cvt_pk_bf16_f32 v47, v228, v230
	v_lshlrev_b32_e32 v250, 16, v47
	v_and_b32_e32 v251, 0xffff0000, v47
	v_sub_f32_e32 v250, v228, v250
	v_sub_f32_e32 v251, v230, v251
	v_cvt_pk_bf16_f32 v51, v250, v251
	v_cvt_pk_bf16_f32 v48, v232, v234
	v_lshlrev_b32_e32 v248, 16, v48
	v_and_b32_e32 v249, 0xffff0000, v48
	v_sub_f32_e32 v248, v232, v248
	v_sub_f32_e32 v249, v234, v249
	v_cvt_pk_bf16_f32 v52, v248, v249
	v_cvt_pk_bf16_f32 v49, v236, v238
	v_lshlrev_b32_e32 v250, 16, v49
	v_and_b32_e32 v251, 0xffff0000, v49
	v_sub_f32_e32 v250, v236, v250
	v_sub_f32_e32 v251, v238, v251
	v_cvt_pk_bf16_f32 v53, v250, v251
	v_cvt_pk_bf16_f32 v18, v225, v227
	v_lshlrev_b32_e32 v248, 16, v18
	v_and_b32_e32 v249, 0xffff0000, v18
	v_sub_f32_e32 v248, v225, v248
	v_sub_f32_e32 v249, v227, v249
	v_cvt_pk_bf16_f32 v14, v248, v249
	v_cvt_pk_bf16_f32 v19, v229, v231
	v_lshlrev_b32_e32 v250, 16, v19
	v_and_b32_e32 v251, 0xffff0000, v19
	v_sub_f32_e32 v250, v229, v250
	v_sub_f32_e32 v251, v231, v251
	v_cvt_pk_bf16_f32 v15, v250, v251
	v_cvt_pk_bf16_f32 v20, v233, v235
	v_lshlrev_b32_e32 v248, 16, v20
	v_and_b32_e32 v249, 0xffff0000, v20
	v_sub_f32_e32 v248, v233, v248
	v_sub_f32_e32 v249, v235, v249
	v_cvt_pk_bf16_f32 v16, v248, v249
	v_cvt_pk_bf16_f32 v21, v237, v239
	v_lshlrev_b32_e32 v250, 16, v21
	v_and_b32_e32 v251, 0xffff0000, v21
	v_sub_f32_e32 v250, v237, v250
	v_sub_f32_e32 v251, v239, v251
	v_cvt_pk_bf16_f32 v17, v250, v251
	v_mov_b32_e32 v113, 0
	v_cmp_gt_u32_e32 vcc, 0x100, v0
	v_and_b32_e32 v115, 63, v0
	v_lshrrev_b32_e32 v125, 2, v115
	v_lshlrev_b32_e32 v114, 2, v0
	v_and_b32_e32 v114, 12, v114
	v_mul_u32_u24_e32 v115, 20, v125
	v_mul_u32_u24_e32 v112, 0xa00, v149
	v_lshlrev_b32_e32 v115, 2, v115
	v_lshlrev_b32_e32 v120, 2, v114
	v_add3_u32 v118, v112, v115, v120
	v_lshlrev_b32_e32 v112, 2, v151
	v_lshl_add_u64 v[114:115], s[26:27], 0, v[112:113]
	v_mov_b32_e32 v112, 0x100
	v_cndmask_b32_e64 v112, v112, 0, vcc
	v_lshl_add_u64 v[122:123], s[28:29], 0, v[112:113]
	v_lshlrev_b32_e32 v112, 1, v153
	v_mov_b32_e32 v121, v113
	v_lshl_add_u64 v[112:113], v[122:123], 0, v[112:113]
	v_lshl_add_u64 v[114:115], v[114:115], 0, v[120:121]
	v_lshl_add_u64 v[112:113], v[112:113], 0, v[120:121]
	v_mul_u32_u24_e32 v120, 0x50, v152
	v_or_b32_e32 v120, v120, v150
	v_and_b32_e32 v124, 48, v0
	s_movk_i32 s4, 0xa00
	v_lshlrev_b32_e32 v120, 2, v120
	v_add_u32_e32 v122, s15, v125
	v_mul_u32_u24_e32 v116, 0x110, v1
	v_mul_u32_u24_e32 v117, 0x110, v146
	v_or_b32_e32 v119, 0xc350, v125
	s_max_u32 s6, s10, 1
	v_mad_u32_u24 v120, v149, s4, v120
	v_mad_u32_u24 v121, v150, s17, v124
	v_add_u32_e32 v122, 0xffffd887, v122
	v_add_u32_e32 v240, 0xcc00, v120
	v_add_u32_e32 v241, 0xd000, v120
	v_mov_b32_e32 v242, v119
	v_mov_b32_e32 v243, 0
	v_lshlrev_b64 v[244:245], 9, v[242:243]
	v_lshl_add_u64 v[228:229], v[114:115], 0, v[244:245]
	v_lshl_add_u64 v[230:231], v[112:113], 0, v[244:245]
	s_branch .LBB0_9

_Z11edge_kernelPK15HIP_vector_typeIjLj2EEPKiPiPS_IiLj2EEPKfPK6__halfPfSD_:
	s_load_dwordx2 s[52:53], s[0:1], 0x0
	s_load_dwordx2 s[54:55], s[0:1], 0x10
	s_load_dwordx8 s[56:63], s[0:1], 0x18
	s_load_dwordx2 s[64:65], s[0:1], 0x38
	v_lshrrev_b32_e32 v112, 6, v0
	v_and_b32_e32 v116, 63, v0
	v_readfirstlane_b32 s38, v112
	v_lshlrev_b32_e32 v116, 4, v116
	v_mov_b32_e32 v117, 0
	s_mul_i32 s39, s2, 0x18800
	s_sub_i32 s38, s38, 2
	s_cmp_lt_i32 s38, 0
	s_cbranch_scc1 .Lq_dma_done
	s_waitcnt lgkmcnt(0)
	s_add_u32 s36, s58, s39
	s_addc_u32 s37, s59, 0

.LBB1_9:
	s_or_b64 exec, exec, s[8:9]
	s_mov_b64 s[24:25], s[52:53]
	s_movk_i32 s3, 0x81
	v_cmp_gt_u32_e32 vcc, s3, v0
	s_waitcnt lgkmcnt(0)
	s_barrier
	s_and_saveexec_b64 s[8:9], vcc
	s_cbranch_execz .LBB1_11
	v_add_u32_e32 v2, 0x10410, v6
	ds_read_b32 v2, v2
	v_add_u32_e32 v3, 0x10c20, v6
	s_waitcnt lgkmcnt(0)
	ds_write_b32 v3, v2

.LBB1_17:
	s_mov_b64 s[26:27], s[54:55]
	s_movk_i32 s3, 0x1000
	s_and_b64 vcc, exec, s[8:9]
	v_cmp_lt_i32_e64 s[8:9], v0, v77
	s_cbranch_vccz .LBB1_40
	v_or_b32_e32 v113, 0x400, v0
	v_or_b32_e32 v114, 0x800, v0
	v_or_b32_e32 v115, 0xc00, v0
	v_mov_b32_e32 v116, 0x10c20
	v_mov_b32_e32 v117, 0x10c20
	v_mov_b32_e32 v118, 0x10c20
	v_mov_b32_e32 v119, 0x10c20
	v_add_u32_e32 v120, 256, v116
	v_add_u32_e32 v121, 256, v117
	v_add_u32_e32 v122, 256, v118
	v_add_u32_e32 v123, 256, v119
	ds_read_b32 v124, v120
	ds_read_b32 v125, v121
	ds_read_b32 v126, v122
	ds_read_b32 v127, v123
	s_waitcnt lgkmcnt(0)
	v_cmp_le_i32_e64 s[36:37], v124, v0
	v_cmp_le_i32_e64 s[38:39], v125, v113
	v_cmp_le_i32_e64 s[40:41], v126, v114
	v_cmp_le_i32_e64 s[42:43], v127, v115
	v_cndmask_b32_e64 v116, v116, v120, s[36:37]
	v_cndmask_b32_e64 v117, v117, v121, s[38:39]
	v_cndmask_b32_e64 v118, v118, v122, s[40:41]
	v_cndmask_b32_e64 v119, v119, v123, s[42:43]
	v_add_u32_e32 v120, 128, v116
	v_add_u32_e32 v121, 128, v117
	v_add_u32_e32 v122, 128, v118
	v_add_u32_e32 v123, 128, v119
	ds_read_b32 v124, v120
	ds_read_b32 v125, v121
	ds_read_b32 v126, v122
	ds_read_b32 v127, v123
	s_waitcnt lgkmcnt(0)
	v_cmp_le_i32_e64 s[36:37], v124, v0
	v_cmp_le_i32_e64 s[38:39], v125, v113
	v_cmp_le_i32_e64 s[40:41], v126, v114
	v_cmp_le_i32_e64 s[42:43], v127, v115
	v_cndmask_b32_e64 v116, v116, v120, s[36:37]
	v_cndmask_b32_e64 v117, v117, v121, s[38:39]
	v_cndmask_b32_e64 v118, v118, v122, s[40:41]
	v_cndmask_b32_e64 v119, v119, v123, s[42:43]
	v_add_u32_e32 v120, 64, v116
	v_add_u32_e32 v121, 64, v117
	v_add_u32_e32 v122, 64, v118
	v_add_u32_e32 v123, 64, v119
	ds_read_b32 v124, v120
	ds_read_b32 v125, v121
	ds_read_b32 v126, v122
	ds_read_b32 v127, v123
	s_waitcnt lgkmcnt(0)
	v_cmp_le_i32_e64 s[36:37], v124, v0
	v_cmp_le_i32_e64 s[38:39], v125, v113
	v_cmp_le_i32_e64 s[40:41], v126, v114
	v_cmp_le_i32_e64 s[42:43], v127, v115
	v_cndmask_b32_e64 v116, v116, v120, s[36:37]
	v_cndmask_b32_e64 v117, v117, v121, s[38:39]
	v_cndmask_b32_e64 v118, v118, v122, s[40:41]
	v_cndmask_b32_e64 v119, v119, v123, s[42:43]
	v_add_u32_e32 v120, 32, v116
	v_add_u32_e32 v121, 32, v117
	v_add_u32_e32 v122, 32, v118
	v_add_u32_e32 v123, 32, v119
	ds_read_b32 v124, v120
	ds_read_b32 v125, v121
	ds_read_b32 v126, v122
	ds_read_b32 v127, v123
	s_waitcnt lgkmcnt(0)
	v_cmp_le_i32_e64 s[36:37], v124, v0
	v_cmp_le_i32_e64 s[38:39], v125, v113
	v_cmp_le_i32_e64 s[40:41], v126, v114
	v_cmp_le_i32_e64 s[42:43], v127, v115
	v_cndmask_b32_e64 v116, v116, v120, s[36:37]
	v_cndmask_b32_e64 v117, v117, v121, s[38:39]
	v_cndmask_b32_e64 v118, v118, v122, s[40:41]
	v_cndmask_b32_e64 v119, v119, v123, s[42:43]
	v_add_u32_e32 v120, 16, v116
	v_add_u32_e32 v121, 16, v117
	v_add_u32_e32 v122, 16, v118
	v_add_u32_e32 v123, 16, v119
	ds_read_b32 v124, v120
	ds_read_b32 v125, v121
	ds_read_b32 v126, v122
	ds_read_b32 v127, v123
	s_waitcnt lgkmcnt(0)
	v_cmp_le_i32_e64 s[36:37], v124, v0
	v_cmp_le_i32_e64 s[38:39], v125, v113
	v_cmp_le_i32_e64 s[40:41], v126, v114
	v_cmp_le_i32_e64 s[42:43], v127, v115
	v_cndmask_b32_e64 v116, v116, v120, s[36:37]
	v_cndmask_b32_e64 v117, v117, v121, s[38:39]
	v_cndmask_b32_e64 v118, v118, v122, s[40:41]
	v_cndmask_b32_e64 v119, v119, v123, s[42:43]
	v_add_u32_e32 v120, 8, v116
	v_add_u32_e32 v121, 8, v117
	v_add_u32_e32 v122, 8, v118
	v_add_u32_e32 v123, 8, v119
	ds_read_b32 v124, v120
	ds_read_b32 v125, v121
	ds_read_b32 v126, v122
	ds_read_b32 v127, v123
	s_waitcnt lgkmcnt(0)
	v_cmp_le_i32_e64 s[36:37], v124, v0
	v_cmp_le_i32_e64 s[38:39], v125, v113
	v_cmp_le_i32_e64 s[40:41], v126, v114
	v_cmp_le_i32_e64 s[42:43], v127, v115
	v_cndmask_b32_e64 v116, v116, v120, s[36:37]
	v_cndmask_b32_e64 v117, v117, v121, s[38:39]
	v_cndmask_b32_e64 v118, v118, v122, s[40:41]
	v_cndmask_b32_e64 v119, v119, v123, s[42:43]
	v_add_u32_e32 v120, 4, v116
	v_add_u32_e32 v121, 4, v117
	v_add_u32_e32 v122, 4, v118
	v_add_u32_e32 v123, 4, v119
	ds_read_b32 v124, v120
	ds_read_b32 v125, v121
	ds_read_b32 v126, v122
	ds_read_b32 v127, v123
	s_waitcnt lgkmcnt(0)
	v_cmp_le_i32_e64 s[36:37], v124, v0
	v_cmp_le_i32_e64 s[38:39], v125, v113
	v_cmp_le_i32_e64 s[40:41], v126, v114
	v_cmp_le_i32_e64 s[42:43], v127, v115
	v_cndmask_b32_e64 v116, v116, v120, s[36:37]
	v_cndmask_b32_e64 v117, v117, v121, s[38:39]
	v_cndmask_b32_e64 v118, v118, v122, s[40:41]
	v_cndmask_b32_e64 v119, v119, v123, s[42:43]
	ds_read_b32 v120, v116
	ds_read_b32 v121, v117
	ds_read_b32 v122, v118
	ds_read_b32 v123, v119
	ds_read_b32 v124, v116 offset:528
	ds_read_b32 v125, v117 offset:528
	ds_read_b32 v126, v118 offset:528
	ds_read_b32 v127, v119 offset:528
	v_cmp_lt_i32_e64 s[10:11], v114, v77
	v_cmp_lt_i32_e64 s[12:13], v115, v77
	s_waitcnt lgkmcnt(0)
	v_add_u32_e32 v124, v124, v0
	v_add_u32_e32 v125, v125, v113
	v_add_u32_e32 v126, v126, v114
	v_add_u32_e32 v127, v127, v115
	v_sub_u32_e32 v116, v124, v120
	v_sub_u32_e32 v118, v125, v121
	v_sub_u32_e32 v120, v126, v122
	v_sub_u32_e32 v122, v127, v123
	v_ashrrev_i32_e32 v117, 31, v116
	v_ashrrev_i32_e32 v119, 31, v118
	v_ashrrev_i32_e32 v121, 31, v120
	v_ashrrev_i32_e32 v123, 31, v122
	v_lshl_add_u64 v[116:117], v[116:117], 3, s[24:25]
	v_lshl_add_u64 v[118:119], v[118:119], 3, s[24:25]
	v_lshl_add_u64 v[120:121], v[120:121], 3, s[24:25]
	v_lshl_add_u64 v[122:123], v[122:123], 3, s[24:25]
	v_cmp_lt_i32_e32 vcc, v113, v77
	s_mov_b64 s[16:17], exec
	s_and_b64 exec, s[16:17], s[8:9]
	global_load_dwordx2 v[42:43], v[116:117], off
	s_and_b64 exec, s[16:17], vcc
	global_load_dwordx2 v[44:45], v[118:119], off
	s_and_b64 exec, s[16:17], s[10:11]
	global_load_dwordx2 v[46:47], v[120:121], off
	s_and_b64 exec, s[16:17], s[12:13]
	global_load_dwordx2 v[48:49], v[122:123], off
	s_mov_b64 exec, s[16:17]

.LBB1_41:
	s_mov_b64 s[16:17], s[56:57]
	s_mov_b64 s[18:19], s[58:59]
	s_mov_b64 s[20:21], s[60:61]
	s_mov_b64 s[22:23], s[62:63]
	s_mov_b64 s[8:9], s[64:65]
	v_cmp_lt_i32_e32 vcc, s3, v77
	s_waitcnt lgkmcnt(0)
	s_barrier
	s_and_saveexec_b64 s[10:11], s[6:7]
	s_cbranch_execz .LBB1_44
	v_lshlrev_b32_e32 v13, 4, v0
	v_add_u32_e32 v7, 0x10820, v13
	ds_read_b128 v[8:11], v7
	s_waitcnt lgkmcnt(0)
	v_add_u32_e32 v15, v9, v8
	v_add3_u32 v11, v15, v10, v11
	v_mov_b32_e32 v7, v11
	s_nop 1
	v_add_u32_dpp v7, v7, v7 row_shr:1 row_mask:0xf bank_mask:0xf
	s_nop 1
	v_add_u32_dpp v7, v7, v7 row_shr:2 row_mask:0xf bank_mask:0xf
	s_nop 1
	v_add_u32_dpp v7, v7, v7 row_shr:4 row_mask:0xf bank_mask:0xf
	s_nop 1
	v_add_u32_dpp v7, v7, v7 row_shr:8 row_mask:0xf bank_mask:0xf
	s_nop 1
	v_add_u32_dpp v7, v7, v7 row_bcast:15 row_mask:0xa bank_mask:0xf
	s_nop 1
	v_add_u32_dpp v7, v7, v7 row_bcast:31 row_mask:0xc bank_mask:0xf
	v_sub_u32_e32 v12, v7, v11
	v_or_b32_e32 v11, 0x10000, v13
	v_add_u32_e32 v13, v12, v8
	v_add_u32_e32 v14, v13, v9
	v_add_u32_e32 v15, v14, v10
	v_cmp_eq_u32_e64 s[0:1], 63, v0
	ds_write_b128 v11, v[12:15]
	s_and_b64 exec, exec, s[0:1]
	v_mov_b32_e32 v8, 0x10400
	ds_write_b32 v8, v7

	.amdhsa_kernel _Z11edge_kernelPK15HIP_vector_typeIjLj2EEPKiPiPS_IiLj2EEPKfPK6__halfPfSD_
		.amdhsa_group_segment_fixed_size 159792
		.amdhsa_private_segment_fixed_size 0
		.amdhsa_kernarg_size 64
		.amdhsa_user_sgpr_count 2
		.amdhsa_user_sgpr_dispatch_ptr 0
		.amdhsa_user_sgpr_queue_ptr 0
		.amdhsa_user_sgpr_kernarg_segment_ptr 1
		.amdhsa_user_sgpr_dispatch_id 0
		.amdhsa_user_sgpr_kernarg_preload_length 0
		.amdhsa_user_sgpr_kernarg_preload_offset 0
		.amdhsa_user_sgpr_private_segment_size 0
		.amdhsa_uses_dynamic_stack 0
		.amdhsa_enable_private_segment 0
		.amdhsa_system_sgpr_workgroup_id_x 1
		.amdhsa_system_sgpr_workgroup_id_y 0
		.amdhsa_system_sgpr_workgroup_id_z 0
		.amdhsa_system_sgpr_workgroup_info 0
		.amdhsa_system_vgpr_workitem_id 0
		.amdhsa_next_free_vgpr 128
		.amdhsa_next_free_sgpr 66
		.amdhsa_accum_offset 128
		.amdhsa_reserve_vcc 1
		.amdhsa_float_round_mode_32 0
		.amdhsa_float_round_mode_16_64 0
		.amdhsa_float_denorm_mode_32 3
		.amdhsa_float_denorm_mode_16_64 3
		.amdhsa_dx10_clamp 1
		.amdhsa_ieee_mode 1
		.amdhsa_fp16_overflow 0
		.amdhsa_tg_split 0
		.amdhsa_exception_fp_ieee_invalid_op 0
		.amdhsa_exception_fp_denorm_src 0
		.amdhsa_exception_fp_ieee_div_zero 0
		.amdhsa_exception_fp_ieee_overflow 0
		.amdhsa_exception_fp_ieee_underflow 0
		.amdhsa_exception_fp_ieee_inexact 0
		.amdhsa_exception_int_div_zero 0
	.end_amdhsa_kernel

amdhsa.kernels:
  - .agpr_count:     0
    .args:
      - .actual_access:  read_only
        .address_space:  global
        .offset:         0
        .size:           8
        .value_kind:     global_buffer
      - .actual_access:  read_only
        .address_space:  global
        .offset:         8
        .size:           8
        .value_kind:     global_buffer
      - .actual_access:  write_only
        .address_space:  global
        .offset:         16
        .size:           8
        .value_kind:     global_buffer
      - .actual_access:  write_only
        .address_space:  global
        .offset:         24
        .size:           8
        .value_kind:     global_buffer
      - .actual_access:  write_only
        .address_space:  global
        .offset:         32
        .size:           8
        .value_kind:     global_buffer
      - .actual_access:  read_only
        .address_space:  global
        .offset:         40
        .size:           8
        .value_kind:     global_buffer
      - .actual_access:  read_only
        .address_space:  global
        .offset:         48
        .size:           8
        .value_kind:     global_buffer
      - .actual_access:  read_only
        .address_space:  global
        .offset:         56
        .size:           8
        .value_kind:     global_buffer
      - .actual_access:  read_only
        .address_space:  global
        .offset:         64
        .size:           8
        .value_kind:     global_buffer
      - .actual_access:  write_only
        .address_space:  global
        .offset:         72
        .size:           8
        .value_kind:     global_buffer
      - .actual_access:  write_only
        .address_space:  global
        .offset:         80
        .size:           8
        .value_kind:     global_buffer
    .group_segment_fixed_size: 72704
    .kernarg_segment_align: 8
    .kernarg_segment_size: 88
    .language:       OpenCL C
    .language_version:
      - 2
      - 0
    .max_flat_workgroup_size: 512
    .name:           _Z9l1_kernelPKiS0_P15HIP_vector_typeIjLj2EEPiS4_PKfS6_S6_S6_PfP6__half
    .private_segment_fixed_size: 0
    .sgpr_count:     76
    .sgpr_spill_count: 0
    .symbol:         _Z9l1_kernelPKiS0_P15HIP_vector_typeIjLj2EEPiS4_PKfS6_S6_S6_PfP6__half.kd
    .uniform_work_group_size: 1
    .uses_dynamic_stack: false
    .vgpr_count:     252
    .vgpr_spill_count: 0
    .wavefront_size: 64
  - .agpr_count:     0
    .args:
      - .actual_access:  read_only
        .address_space:  global
        .offset:         0
        .size:           8
        .value_kind:     global_buffer
      - .actual_access:  read_only
        .address_space:  global
        .offset:         8
        .size:           8
        .value_kind:     global_buffer
      - .address_space:  global
        .offset:         16
        .size:           8
        .value_kind:     global_buffer
      - .address_space:  global
        .offset:         24
        .size:           8
        .value_kind:     global_buffer
      - .actual_access:  read_only
        .address_space:  global
        .offset:         32
        .size:           8
        .value_kind:     global_buffer
      - .actual_access:  read_only
        .address_space:  global
        .offset:         40
        .size:           8
        .value_kind:     global_buffer
      - .actual_access:  write_only
        .address_space:  global
        .offset:         48
        .size:           8
        .value_kind:     global_buffer
      - .actual_access:  write_only
        .address_space:  global
        .offset:         56
        .size:           8
        .value_kind:     global_buffer
    .group_segment_fixed_size: 159792
    .kernarg_segment_align: 8
    .kernarg_segment_size: 64
    .language:       OpenCL C
    .language_version:
      - 2
      - 0
    .max_flat_workgroup_size: 1024
    .name:           _Z11edge_kernelPK15HIP_vector_typeIjLj2EEPKiPiPS_IiLj2EEPKfPK6__halfPfSD_
    .private_segment_fixed_size: 0
    .sgpr_count:     72
    .sgpr_spill_count: 0
    .symbol:         _Z11edge_kernelPK15HIP_vector_typeIjLj2EEPKiPiPS_IiLj2EEPKfPK6__halfPfSD_.kd
    .uniform_work_group_size: 1
    .uses_dynamic_stack: false
    .vgpr_count:     128
    .vgpr_spill_count: 0
    .wavefront_size: 64
